# band attention: the eight bias LDS reads issued together before the QK MFMA chain instead of one read-wait-use at a time
# baseline (speedup 1.0000x reference)
.LBB0_1265:
	s_waitcnt vmcnt(0)
	v_mfma_f32_32x32x16_bf16 v[52:67], v[144:147], v[124:127], 0
	ds_write_b128 v191, v[128:131] offset:32768
	ds_write_b128 v191, v[120:123] offset:33280
	ds_write_b128 v191, v[104:107] offset:33792
	ds_write_b128 v191, v[100:103] offset:34304
	ds_read2_b32 v[198:199], v153 offset0:26 offset1:27
	ds_read2_b32 v[208:209], v153 offset0:24 offset1:25
	ds_read2_b32 v[210:211], v153 offset0:18 offset1:19
	ds_read2_b32 v[212:213], v153 offset0:16 offset1:17
	ds_read2_b32 v[214:215], v153 offset0:10 offset1:11
	ds_read2_b32 v[216:217], v153 offset0:8 offset1:9
	ds_read2_b32 v[218:219], v153 offset0:2 offset1:3
	ds_read2_b32 v[220:221], v153 offset1:1
	s_and_b64 vcc, exec, s[60:61]
	v_mfma_f32_32x32x16_bf16 v[52:67], v[140:143], v[116:119], v[52:67]
	v_mfma_f32_32x32x16_bf16 v[52:67], v[136:139], v[112:115], v[52:67]
	v_mfma_f32_32x32x16_bf16 v[52:67], v[132:135], v[108:111], v[52:67]
	s_cbranch_vccnz .Lband_nopf
	global_load_dwordx4 v[144:147], v[180:181], off
	global_load_dwordx4 v[140:143], v[180:181], off offset:32
	global_load_dwordx4 v[136:139], v[180:181], off offset:64
	global_load_dwordx4 v[132:135], v[180:181], off offset:96
	global_load_dwordx4 v[128:131], v[178:179], off
	global_load_dwordx4 v[120:123], v[176:177], off
	global_load_dwordx4 v[104:107], v[174:175], off
	global_load_dwordx4 v[100:103], v[172:173], off
.Lband_nopf:
	s_waitcnt lgkmcnt(0)
	s_nop 10
	v_fmamk_f32 v197, v52, 0x3e38aa3b, v199
	v_fmac_f32_e32 v198, 0x3e38aa3b, v53
	v_max3_f32 v195, v197, s33, v198
	v_fmamk_f32 v53, v54, 0x3e38aa3b, v209
	v_fmamk_f32 v52, v55, 0x3e38aa3b, v208
	v_max3_f32 v195, v195, v53, v52
	v_fmamk_f32 v55, v56, 0x3e38aa3b, v211
	v_fmamk_f32 v54, v57, 0x3e38aa3b, v210
	v_max3_f32 v195, v195, v55, v54
	v_fmamk_f32 v57, v58, 0x3e38aa3b, v213
	v_fmamk_f32 v56, v59, 0x3e38aa3b, v212
	v_max3_f32 v195, v195, v57, v56
	v_fmamk_f32 v59, v60, 0x3e38aa3b, v215
	v_fmamk_f32 v58, v61, 0x3e38aa3b, v214
	v_max3_f32 v195, v195, v59, v58
	v_fmamk_f32 v61, v62, 0x3e38aa3b, v217
	v_fmamk_f32 v60, v63, 0x3e38aa3b, v216
	v_max3_f32 v195, v195, v61, v60
	v_fmamk_f32 v63, v64, 0x3e38aa3b, v219
	v_fmamk_f32 v62, v65, 0x3e38aa3b, v218
	v_max3_f32 v195, v195, v63, v62
	v_fmamk_f32 v65, v66, 0x3e38aa3b, v221
	v_fmamk_f32 v64, v67, 0x3e38aa3b, v220
	v_max3_f32 v66, v195, v65, v64
	v_mov_b32_e32 v67, v66
	s_nop 1
	v_permlane32_swap_b32_e32 v66, v67
	v_max3_f32 v195, v196, v66, v67
	v_sub_f32_e32 v67, v197, v195
	v_exp_f32_e32 v67, v67
	v_sub_f32_e32 v197, v198, v195
	v_exp_f32_e32 v197, v197
	v_sub_f32_e32 v53, v53, v195
	v_exp_f32_e32 v53, v53
	v_sub_f32_e32 v52, v52, v195
	v_exp_f32_e32 v52, v52
	v_sub_f32_e32 v55, v55, v195
	v_sub_f32_e32 v66, v196, v195
	v_add_f32_e32 v196, 0, v67
	v_exp_f32_e32 v55, v55
	v_sub_f32_e32 v54, v54, v195
	v_add_f32_e32 v196, v197, v196
	v_exp_f32_e32 v54, v54
	v_sub_f32_e32 v57, v57, v195
	v_add_f32_e32 v196, v53, v196
	v_exp_f32_e32 v198, v57
	v_add_f32_e32 v196, v52, v196
	v_add_f32_e32 v196, v55, v196
	v_add_f32_e32 v196, v54, v196
	v_sub_f32_e32 v56, v56, v195
	v_add_f32_e32 v57, v198, v196
	v_exp_f32_e32 v196, v56
	s_nop 0
	v_add_f32_e32 v56, v196, v57
	v_sub_f32_e32 v57, v59, v195
	v_exp_f32_e32 v59, v57
	v_sub_f32_e32 v57, v58, v195
	v_exp_f32_e32 v199, v57
	v_sub_f32_e32 v57, v61, v195
	v_exp_f32_e32 v200, v57
	v_sub_f32_e32 v57, v60, v195
	v_exp_f32_e32 v201, v57
	v_sub_f32_e32 v57, v63, v195
	v_add_f32_e32 v56, v59, v56
	v_exp_f32_e32 v202, v57
	v_sub_f32_e32 v57, v62, v195
	v_add_f32_e32 v56, v199, v56
	v_exp_f32_e32 v203, v57
	v_sub_f32_e32 v57, v65, v195
	v_add_f32_e32 v56, v200, v56
	v_exp_f32_e32 v65, v57
	v_sub_f32_e32 v57, v64, v195
	v_add_f32_e32 v56, v201, v56
	v_exp_f32_e32 v64, v57
	v_add_f32_e32 v56, v202, v56
	v_add_f32_e32 v56, v203, v56
	v_add_f32_e32 v56, v65, v56
	v_add_f32_e32 v57, v64, v56
	v_exp_f32_e32 v56, v66
	v_cvt_pk_bf16_f32 v60, v67, v197
	v_cvt_pk_bf16_f32 v62, v55, v54
	v_cvt_pk_bf16_f32 v55, v65, v64
	ds_read_b64_tr_b16 v[64:65], v192 offset:32768
	ds_read_b64_tr_b16 v[66:67], v192 offset:33280
	v_mov_b32_e32 v58, v57
	s_nop 1
	v_permlane32_swap_b32_e32 v57, v58
	v_pk_mul_f32 v[34:35], v[34:35], v[56:57] op_sel_hi:[1,0]
	v_pk_mul_f32 v[32:33], v[32:33], v[56:57] op_sel_hi:[1,0]
	v_pk_mul_f32 v[30:31], v[30:31], v[56:57] op_sel_hi:[1,0]
	v_pk_mul_f32 v[28:29], v[28:29], v[56:57] op_sel_hi:[1,0]
	v_pk_mul_f32 v[26:27], v[26:27], v[56:57] op_sel_hi:[1,0]
	v_pk_mul_f32 v[24:25], v[24:25], v[56:57] op_sel_hi:[1,0]
	v_pk_mul_f32 v[22:23], v[22:23], v[56:57] op_sel_hi:[1,0]
	v_pk_mul_f32 v[20:21], v[20:21], v[56:57] op_sel_hi:[1,0]
	v_cvt_pk_bf16_f32 v61, v53, v52
	v_cvt_pk_bf16_f32 v63, v198, v196
	v_cvt_pk_bf16_f32 v52, v59, v199
	v_cvt_pk_bf16_f32 v53, v200, v201
	v_cvt_pk_bf16_f32 v54, v202, v203
	v_pk_mul_f32 v[50:51], v[50:51], v[56:57] op_sel_hi:[1,0]
	s_waitcnt lgkmcnt(0)
	v_mfma_f32_32x32x16_bf16 v[20:35], v[64:67], v[60:63], v[20:35]
	ds_read_b64_tr_b16 v[64:65], v192 offset:33792
	ds_read_b64_tr_b16 v[66:67], v192 offset:34304
	v_mul_f32_e64 v48, v48, v56
	v_mul_f32_e64 v49, v49, v56
	v_mul_f32_e64 v46, v46, v56
	v_mul_f32_e64 v47, v47, v56
	v_pk_mul_f32 v[44:45], v[44:45], v[56:57] op_sel_hi:[1,0]
	v_pk_mul_f32 v[42:43], v[42:43], v[56:57] op_sel_hi:[1,0]
	v_pk_mul_f32 v[40:41], v[40:41], v[56:57] op_sel_hi:[1,0]
	v_pk_mul_f32 v[38:39], v[38:39], v[56:57] op_sel_hi:[1,0]
	s_waitcnt lgkmcnt(0)
	v_mfma_f32_32x32x16_bf16 v[20:35], v[64:67], v[52:55], v[20:35]
	ds_read_b64_tr_b16 v[64:65], v192 offset:34816
	ds_read_b64_tr_b16 v[66:67], v192 offset:35328
	v_mul_f32_e64 v36, v36, v56
	v_mul_f32_e64 v37, v37, v56
	s_waitcnt lgkmcnt(0)
	s_nop 0
	v_mfma_f32_32x32x16_bf16 v[36:51], v[64:67], v[60:63], v[36:51]
	ds_read_b64_tr_b16 v[60:61], v192 offset:35840
	ds_read_b64_tr_b16 v[62:63], v192 offset:36352
	s_waitcnt lgkmcnt(0)
	v_mfma_f32_32x32x16_bf16 v[36:51], v[60:63], v[52:55], v[36:51]
